# speedup vs baseline: 1.0294x; 1.0129x over previous
.LBB3_8:
	s_and_b64 vcc, exec, s[8:9]
	s_cbranch_vccz .LBB3_11
	s_load_dwordx4 s[8:11], s[0:1], 0x38
	s_load_dwordx2 s[16:17], s[0:1], 0x48
	s_lshl_b32 s2, s2, 5
	v_or_b32_e32 v2, s2, v198
	v_ashrrev_i32_e32 v3, 31, v2
	v_lshlrev_b64 v[2:3], 9, v[2:3]
	v_lshl_or_b32 v230, v197, 5, v198
	v_lshlrev_b32_e32 v230, 2, v230
	s_waitcnt lgkmcnt(0)
	global_load_dword v230, v230, s[16:17]
	v_lshl_add_u64 v[2:3], s[8:9], 0, v[2:3]
	v_lshlrev_b32_e32 v66, 4, v199
	v_mov_b32_e32 v67, 0
	v_lshl_add_u64 v[2:3], v[2:3], 0, v[66:67]
	global_load_dwordx4 v[4:7], v[2:3], off
	v_and_b32_e32 v56, 0xc000, v202
	v_or_b32_e32 v8, v56, v201
	v_lshlrev_b32_e32 v48, 1, v8
	global_load_dwordx4 v[8:11], v48, s[10:11]
	v_or_b32_e32 v57, 0x2000, v56
	v_or_b32_e32 v12, v57, v201
	v_lshlrev_b32_e32 v49, 1, v12
	global_load_dwordx4 v[12:15], v49, s[10:11]
	global_load_dwordx4 v[16:19], v[2:3], off offset:32
	global_load_dwordx4 v[20:23], v48, s[10:11] offset:1024
	v_or_b32_e32 v36, 0x400, v49
	global_load_dwordx4 v[24:27], v36, s[10:11]
	global_load_dwordx4 v[28:31], v[2:3], off offset:64
	global_load_dwordx4 v[32:35], v48, s[10:11] offset:2048
	v_or_b32_e32 v50, 0x800, v49
	global_load_dwordx4 v[36:39], v50, s[10:11]
	global_load_dwordx4 v[40:43], v[2:3], off offset:96
	global_load_dwordx4 v[44:47], v48, s[10:11] offset:3072
	v_or_b32_e32 v48, 0xc00, v49
	global_load_dwordx4 v[48:51], v48, s[10:11]
	v_or_b32_e32 v58, 0x800, v201
	global_load_dwordx4 v[52:55], v[2:3], off offset:128
	v_or_b32_e32 v59, v58, v56
	v_lshlrev_b32_e32 v59, 1, v59
	v_or_b32_e32 v58, v57, v58
	v_lshlrev_b32_e32 v58, 1, v58
	global_load_dwordx4 v[72:75], v[2:3], off offset:448
	global_load_dwordx4 v[76:79], v[2:3], off offset:480
	s_movk_i32 s8, 0x1000
	s_movk_i32 s3, 0x2000
	v_mul_u32_u24_e32 v102, 0x840, v199
	s_waitcnt vmcnt(13)
	v_mfma_f32_32x32x16_f16 a[16:31], v[4:7], v[8:11], 0
	global_load_dwordx4 v[8:11], v59, s[10:11]
	global_load_dwordx4 v[68:71], v[2:3], off offset:416
	s_waitcnt vmcnt(14)
	v_mfma_f32_32x32x16_f16 a[0:15], v[4:7], v[12:15], 0
	global_load_dwordx4 v[4:7], v58, s[10:11]
	global_load_dwordx4 v[12:15], v[2:3], off offset:160
	v_or_b32_e32 v58, 0xa00, v201
	v_or_b32_e32 v59, v58, v56
	v_lshlrev_b32_e32 v59, 1, v59
	v_or_b32_e32 v58, v57, v58
	v_lshlrev_b32_e32 v58, 1, v58
	s_waitcnt vmcnt(14)
	v_mfma_f32_32x32x16_f16 a[16:31], v[16:19], v[20:23], a[16:31]
	global_load_dwordx4 v[20:23], v59, s[10:11]
	s_waitcnt vmcnt(14)
	v_mfma_f32_32x32x16_f16 a[0:15], v[16:19], v[24:27], a[0:15]
	global_load_dwordx4 v[16:19], v58, s[10:11]
	global_load_dwordx4 v[24:27], v[2:3], off offset:192
	v_or_b32_e32 v58, 0xc00, v201
	v_or_b32_e32 v59, v58, v56
	v_lshlrev_b32_e32 v59, 1, v59
	v_or_b32_e32 v58, v57, v58
	v_lshlrev_b32_e32 v58, 1, v58
	s_waitcnt vmcnt(14)
	v_mfma_f32_32x32x16_f16 a[16:31], v[28:31], v[32:35], a[16:31]
	global_load_dwordx4 v[32:35], v59, s[10:11]
	s_waitcnt vmcnt(14)
	v_mfma_f32_32x32x16_f16 a[0:15], v[28:31], v[36:39], a[0:15]
	global_load_dwordx4 v[36:39], v[2:3], off offset:224
	global_load_dwordx4 v[28:31], v58, s[10:11]
	v_or_b32_e32 v58, 0xe00, v201
	v_or_b32_e32 v59, v58, v56
	v_lshlrev_b32_e32 v59, 1, v59
	v_or_b32_e32 v58, v57, v58
	v_lshlrev_b32_e32 v58, 1, v58
	s_waitcnt vmcnt(14)
	v_mfma_f32_32x32x16_f16 a[16:31], v[40:43], v[44:47], a[16:31]
	global_load_dwordx4 v[44:47], v59, s[10:11]
	s_waitcnt vmcnt(14)
	v_mfma_f32_32x32x16_f16 a[0:15], v[40:43], v[48:51], a[0:15]
	global_load_dwordx4 v[48:51], v[2:3], off offset:256
	global_load_dwordx4 v[40:43], v58, s[10:11]
	v_or_b32_e32 v58, 0x1000, v201
	v_or_b32_e32 v59, v58, v56
	v_lshlrev_b32_e32 v59, 1, v59
	v_or_b32_e32 v58, v57, v58
	v_lshlrev_b32_e32 v58, 1, v58
	s_waitcnt vmcnt(12)
	v_mfma_f32_32x32x16_f16 a[16:31], v[52:55], v[8:11], a[16:31]
	global_load_dwordx4 v[8:11], v59, s[10:11]
	s_waitcnt vmcnt(11)
	v_mfma_f32_32x32x16_f16 a[0:15], v[52:55], v[4:7], a[0:15]
	global_load_dwordx4 v[52:55], v[2:3], off offset:288
	global_load_dwordx4 v[4:7], v58, s[10:11]
	v_or_b32_e32 v58, 0x1200, v201
	v_or_b32_e32 v59, v58, v56
	v_lshlrev_b32_e32 v59, 1, v59
	v_or_b32_e32 v58, v57, v58
	v_lshlrev_b32_e32 v58, 1, v58
	s_waitcnt vmcnt(11)
	v_mfma_f32_32x32x16_f16 a[16:31], v[12:15], v[20:23], a[16:31]
	global_load_dwordx4 v[20:23], v59, s[10:11]
	s_waitcnt vmcnt(11)
	v_mfma_f32_32x32x16_f16 a[0:15], v[12:15], v[16:19], a[0:15]
	global_load_dwordx4 v[12:15], v58, s[10:11]
	global_load_dwordx4 v[16:19], v[2:3], off offset:320
	s_waitcnt vmcnt(11)
	v_mfma_f32_32x32x16_f16 a[16:31], v[24:27], v[32:35], a[16:31]
	s_waitcnt vmcnt(9)
	v_mfma_f32_32x32x16_f16 a[0:15], v[24:27], v[28:31], a[0:15]
	global_load_dwordx4 v[28:31], v[2:3], off offset:352
	s_waitcnt vmcnt(9)
	v_mfma_f32_32x32x16_f16 a[16:31], v[36:39], v[44:47], a[16:31]
	s_waitcnt vmcnt(7)
	v_mfma_f32_32x32x16_f16 a[0:15], v[36:39], v[40:43], a[0:15]
	global_load_dwordx4 v[40:43], v[2:3], off offset:384
	v_mov_b32_e32 v3, v67
	v_and_b32_e32 v67, 0xdf, v0
	v_or_b32_e32 v0, 32, v0
	s_waitcnt vmcnt(7)
	v_mfma_f32_32x32x16_f16 a[16:31], v[48:51], v[8:11], a[16:31]
	s_waitcnt vmcnt(5)
	v_mfma_f32_32x32x16_f16 a[0:15], v[48:51], v[4:7], a[0:15]
	v_or_b32_e32 v48, 0x1a00, v201
	v_or_b32_e32 v49, v48, v56
	v_lshlrev_b32_e32 v49, 1, v49
	s_waitcnt vmcnt(4)
	v_mfma_f32_32x32x16_f16 a[16:31], v[52:55], v[20:23], a[16:31]
	global_load_dwordx4 v[20:23], v49, s[10:11]
	v_or_b32_e32 v58, 0x1400, v201
	v_or_b32_e32 v59, v58, v56
	v_or_b32_e32 v58, v57, v58
	v_lshlrev_b32_e32 v59, 1, v59
	v_lshlrev_b32_e32 v58, 1, v58
	v_or_b32_e32 v49, 0x1c00, v201
	global_load_dwordx4 v[32:35], v59, s[10:11]
	global_load_dwordx4 v[24:27], v58, s[10:11]
	v_or_b32_e32 v50, v49, v56
	v_lshlrev_b32_e32 v50, 1, v50
	s_waitcnt vmcnt(6)
	v_mfma_f32_32x32x16_f16 a[0:15], v[52:55], v[12:15], a[0:15]
	global_load_dwordx4 v[12:15], v50, s[10:11]
	v_or_b32_e32 v50, 0x1e00, v201
	v_or_b32_e32 v2, v50, v56
	v_lshlrev_b32_e32 v2, 1, v2
	global_load_dwordx4 v[62:65], v2, s[10:11]
	v_or_b32_e32 v58, 0x1600, v201
	v_or_b32_e32 v59, v58, v56
	v_or_b32_e32 v58, v57, v58
	v_lshlrev_b32_e32 v59, 1, v59
	v_lshlrev_b32_e32 v58, 1, v58
	global_load_dwordx4 v[44:47], v59, s[10:11]
	global_load_dwordx4 v[36:39], v58, s[10:11]
	v_or_b32_e32 v2, v57, v48
	v_lshlrev_b32_e32 v2, 1, v2
	global_load_dwordx4 v[80:83], v2, s[10:11]
	v_or_b32_e32 v58, 0x1800, v201
	v_or_b32_e32 v59, v58, v56
	v_or_b32_e32 v58, v57, v58
	v_lshlrev_b32_e32 v59, 1, v59
	v_lshlrev_b32_e32 v58, 1, v58
	global_load_dwordx4 v[8:11], v59, s[10:11]
	global_load_dwordx4 v[4:7], v58, s[10:11]
	v_or_b32_e32 v2, v57, v49
	v_lshlrev_b32_e32 v2, 1, v2
	global_load_dwordx4 v[84:87], v2, s[10:11]
	v_or_b32_e32 v2, v57, v50
	v_lshlrev_b32_e32 v2, 1, v2
	global_load_dwordx4 v[88:91], v2, s[10:11]
	v_lshl_or_b32 v2, v197, 14, v200
	s_waitcnt vmcnt(10)
	v_mfma_f32_32x32x16_f16 a[16:31], v[16:19], v[32:35], a[16:31]
	s_waitcnt vmcnt(9)
	v_mfma_f32_32x32x16_f16 a[0:15], v[16:19], v[24:27], a[0:15]
	s_waitcnt vmcnt(6)
	v_mfma_f32_32x32x16_f16 a[16:31], v[28:31], v[44:47], a[16:31]
	s_waitcnt vmcnt(5)
	v_mfma_f32_32x32x16_f16 a[0:15], v[28:31], v[36:39], a[0:15]
	s_waitcnt vmcnt(3)
	v_mfma_f32_32x32x16_f16 a[16:31], v[40:43], v[8:11], a[16:31]
	v_lshl_add_u64 v[8:9], s[6:7], 0, v[2:3]
	v_lshlrev_b32_e32 v3, 2, v67
	global_load_dword v92, v3, s[4:5]
	v_lshl_add_u32 v67, v67, 1, v102
	s_waitcnt vmcnt(3)
	v_mfma_f32_32x32x16_f16 a[0:15], v[40:43], v[4:7], a[0:15]
	global_load_dwordx4 v[58:61], v2, s[6:7]
	global_load_dwordx4 v[50:53], v2, s[6:7] offset:1024
	global_load_dwordx4 v[42:45], v2, s[6:7] offset:2048
	global_load_dwordx4 v[38:41], v2, s[6:7] offset:3072
	v_add_co_u32_e32 v2, vcc, s8, v8
	s_nop 1
	v_addc_co_u32_e32 v3, vcc, 0, v9, vcc
	v_add_co_u32_e32 v4, vcc, s3, v8
	v_mfma_f32_32x32x16_f16 a[16:31], v[68:71], v[20:23], a[16:31]
	s_nop 0
	v_addc_co_u32_e32 v5, vcc, 0, v9, vcc
	s_movk_i32 s3, 0x3000
	global_load_dwordx4 v[46:49], v[2:3], off offset:1024
	global_load_dwordx4 v[34:37], v[2:3], off offset:2048
	global_load_dwordx4 v[54:57], v[4:5], off offset:-4096
	global_load_dwordx4 v[26:29], v[4:5], off
	v_mfma_f32_32x32x16_f16 a[0:15], v[68:71], v[80:83], a[0:15]
	v_mfma_f32_32x32x16_f16 a[16:31], v[72:75], v[12:15], a[16:31]
	global_load_dwordx4 v[30:33], v[4:5], off offset:1024
	global_load_dwordx4 v[14:17], v[4:5], off offset:2048
	global_load_dwordx4 v[10:13], v[4:5], off offset:3072
	v_add_co_u32_e32 v4, vcc, s3, v8
	s_movk_i32 s3, 0x210
	s_nop 0
	v_addc_co_u32_e32 v5, vcc, 0, v9, vcc
	s_waitcnt vmcnt(13)
	v_mfma_f32_32x32x16_f16 a[0:15], v[72:75], v[84:87], a[0:15]
	v_mfma_f32_32x32x16_f16 a[16:31], v[76:79], v[62:65], a[16:31]
	global_load_dwordx4 v[62:65], v[2:3], off offset:3072
	global_load_dwordx4 v[22:25], v[4:5], off
	global_load_dwordx4 v[18:21], v[4:5], off offset:1024
	global_load_dwordx4 v[6:9], v[4:5], off offset:2048
	s_nop 0
	global_load_dwordx4 v[2:5], v[4:5], off offset:3072
	s_nop 5
	v_accvgpr_read_b32 v93, a16
	s_waitcnt vmcnt(17)
	v_mfma_f32_32x32x16_f16 a[0:15], v[76:79], v[88:91], a[0:15]
	v_lshlrev_b32_e32 v79, 2, v0
	global_load_dword v79, v79, s[4:5]
	v_accvgpr_read_b32 v94, a17
	v_accvgpr_read_b32 v68, a18
	v_accvgpr_read_b32 v69, a19
	v_accvgpr_read_b32 v70, a20
	v_accvgpr_read_b32 v71, a21
	v_accvgpr_read_b32 v80, a22
	v_accvgpr_read_b32 v81, a23
	v_accvgpr_read_b32 v82, a24
	v_accvgpr_read_b32 v72, a25
	v_accvgpr_read_b32 v73, a26
	v_accvgpr_read_b32 v74, a27
	v_accvgpr_read_b32 v75, a28
	v_accvgpr_read_b32 v83, a29
	v_accvgpr_read_b32 v84, a30
	v_accvgpr_read_b32 v85, a31
	v_accvgpr_read_b32 v76, a0
	v_accvgpr_read_b32 v77, a1
	v_accvgpr_read_b32 v78, a2
	v_accvgpr_read_b32 v86, a3
	v_accvgpr_read_b32 v87, a4
	v_lshl_add_u32 v0, v0, 1, v102
	v_accvgpr_read_b32 v88, a5
	s_waitcnt vmcnt(17)
	v_add_f32_e32 v93, v93, v92
	v_max_f32_e32 v93, 0, v93
	v_add_f32_e32 v94, v94, v92
	v_cvt_f16_f32_e32 v93, v93
	v_max_f32_e32 v94, 0, v94
	v_add_f32_e32 v68, v68, v92
	v_cvt_f16_f32_e32 v94, v94
	v_max_f32_e32 v68, 0, v68
	v_add_f32_e32 v69, v69, v92
	v_cvt_f16_f32_e32 v68, v68
	v_max_f32_e32 v69, 0, v69
	v_cvt_f16_f32_e32 v69, v69
	ds_write_b16 v67, v93
	ds_write_b16 v67, v94 offset:528
	ds_write_b16 v67, v68 offset:1056
	ds_write_b16 v67, v69 offset:1584
	v_add_f32_e32 v68, v70, v92
	v_max_f32_e32 v68, 0, v68
	v_add_f32_e32 v69, v71, v92
	v_cvt_f16_f32_e32 v68, v68
	v_max_f32_e32 v69, 0, v69
	v_add_f32_e32 v70, v80, v92
	v_cvt_f16_f32_e32 v69, v69
	v_max_f32_e32 v70, 0, v70
	v_add_f32_e32 v71, v81, v92
	v_cvt_f16_f32_e32 v70, v70
	v_max_f32_e32 v71, 0, v71
	v_cvt_f16_f32_e32 v71, v71
	ds_write_b16 v67, v68 offset:4224
	ds_write_b16 v67, v69 offset:4752
	ds_write_b16 v67, v70 offset:5280
	ds_write_b16 v67, v71 offset:5808
	v_add_f32_e32 v68, v82, v92
	v_max_f32_e32 v68, 0, v68
	v_add_f32_e32 v69, v72, v92
	v_cvt_f16_f32_e32 v68, v68
	v_max_f32_e32 v69, 0, v69
	v_add_f32_e32 v70, v73, v92
	v_cvt_f16_f32_e32 v69, v69
	v_max_f32_e32 v70, 0, v70
	v_add_f32_e32 v71, v74, v92
	v_cvt_f16_f32_e32 v70, v70
	v_max_f32_e32 v71, 0, v71
	v_cvt_f16_f32_e32 v71, v71
	ds_write_b16 v67, v68 offset:8448
	ds_write_b16 v67, v69 offset:8976
	ds_write_b16 v67, v70 offset:9504
	ds_write_b16 v67, v71 offset:10032
	v_add_f32_e32 v68, v75, v92
	v_max_f32_e32 v68, 0, v68
	v_add_f32_e32 v69, v83, v92
	v_cvt_f16_f32_e32 v68, v68
	v_max_f32_e32 v69, 0, v69
	v_add_f32_e32 v70, v84, v92
	v_cvt_f16_f32_e32 v69, v69
	v_max_f32_e32 v70, 0, v70
	v_add_f32_e32 v71, v85, v92
	v_cvt_f16_f32_e32 v70, v70
	v_max_f32_e32 v71, 0, v71
	v_cvt_f16_f32_e32 v71, v71
	ds_write_b16 v67, v68 offset:12672
	ds_write_b16 v67, v69 offset:13200
	ds_write_b16 v67, v70 offset:13728
	ds_write_b16 v67, v71 offset:14256
	v_accvgpr_read_b32 v89, a6
	v_accvgpr_read_b32 v90, a7
	v_accvgpr_read_b32 v91, a8
	v_accvgpr_read_b32 v95, a9
	v_accvgpr_read_b32 v96, a10
	s_waitcnt vmcnt(0)
	v_add_f32_e32 v67, v76, v79
	v_max_f32_e32 v67, 0, v67
	v_add_f32_e32 v68, v77, v79
	v_cvt_f16_f32_e32 v67, v67
	v_max_f32_e32 v68, 0, v68
	v_add_f32_e32 v69, v78, v79
	v_cvt_f16_f32_e32 v68, v68
	v_max_f32_e32 v69, 0, v69
	v_add_f32_e32 v70, v86, v79
	v_cvt_f16_f32_e32 v69, v69
	v_max_f32_e32 v70, 0, v70
	v_cvt_f16_f32_e32 v70, v70
	ds_write_b16 v0, v67
	ds_write_b16 v0, v68 offset:528
	ds_write_b16 v0, v69 offset:1056
	ds_write_b16 v0, v70 offset:1584
	v_add_f32_e32 v67, v87, v79
	v_max_f32_e32 v67, 0, v67
	v_add_f32_e32 v68, v88, v79
	v_cvt_f16_f32_e32 v67, v67
	v_max_f32_e32 v68, 0, v68
	v_add_f32_e32 v69, v89, v79
	v_cvt_f16_f32_e32 v68, v68
	v_max_f32_e32 v69, 0, v69
	v_add_f32_e32 v70, v90, v79
	v_cvt_f16_f32_e32 v69, v69
	v_max_f32_e32 v70, 0, v70
	v_cvt_f16_f32_e32 v70, v70
	ds_write_b16 v0, v67 offset:4224
	ds_write_b16 v0, v68 offset:4752
	ds_write_b16 v0, v69 offset:5280
	ds_write_b16 v0, v70 offset:5808
	v_add_f32_e32 v67, v91, v79
	v_max_f32_e32 v67, 0, v67
	v_add_f32_e32 v68, v95, v79
	v_accvgpr_read_b32 v97, a11
	v_cvt_f16_f32_e32 v67, v67
	v_max_f32_e32 v68, 0, v68
	v_add_f32_e32 v69, v96, v79
	v_cvt_f16_f32_e32 v68, v68
	v_max_f32_e32 v69, 0, v69
	v_add_f32_e32 v70, v97, v79
	v_cvt_f16_f32_e32 v69, v69
	v_max_f32_e32 v70, 0, v70
	v_accvgpr_read_b32 v98, a12
	v_cvt_f16_f32_e32 v70, v70
	v_accvgpr_read_b32 v99, a13
	ds_write_b16 v0, v67 offset:8448
	ds_write_b16 v0, v68 offset:8976
	ds_write_b16 v0, v69 offset:9504
	ds_write_b16 v0, v70 offset:10032
	v_add_f32_e32 v67, v98, v79
	v_accvgpr_read_b32 v100, a14
	v_max_f32_e32 v67, 0, v67
	v_add_f32_e32 v68, v99, v79
	v_accvgpr_read_b32 v101, a15
	v_cvt_f16_f32_e32 v67, v67
	v_max_f32_e32 v68, 0, v68
	v_add_f32_e32 v69, v100, v79
	v_cvt_f16_f32_e32 v68, v68
	v_max_f32_e32 v69, 0, v69
	v_add_f32_e32 v70, v101, v79
	v_cvt_f16_f32_e32 v69, v69
	v_max_f32_e32 v70, 0, v70
	v_cvt_f16_f32_e32 v70, v70
	ds_write_b16 v0, v67 offset:12672
	ds_write_b16 v0, v68 offset:13200
	ds_write_b16 v0, v69 offset:13728
	ds_write_b16 v0, v70 offset:14256
	v_mad_u32_u24 v0, v198, s3, v66
	s_waitcnt lgkmcnt(0)
	s_barrier
	ds_read_b128 v[66:69], v0
	ds_read_b128 v[70:73], v0 offset:32
	s_waitcnt lgkmcnt(1)
	v_mfma_f32_32x32x16_f16 a[0:15], v[66:69], v[58:61], 0
	s_waitcnt lgkmcnt(0)
	v_mfma_f32_32x32x16_f16 a[0:15], v[70:73], v[50:53], a[0:15]
	ds_read_b128 v[50:53], v0 offset:64
	ds_read_b128 v[58:61], v0 offset:96
	s_waitcnt lgkmcnt(1)
	v_mfma_f32_32x32x16_f16 a[0:15], v[50:53], v[42:45], a[0:15]
	s_waitcnt lgkmcnt(0)
	v_mfma_f32_32x32x16_f16 a[0:15], v[58:61], v[38:41], a[0:15]
	ds_read_b128 v[38:41], v0 offset:128
	ds_read_b128 v[42:45], v0 offset:160
	s_waitcnt lgkmcnt(1)
	v_mfma_f32_32x32x16_f16 a[0:15], v[38:41], v[54:57], a[0:15]
	s_waitcnt lgkmcnt(0)
	v_mfma_f32_32x32x16_f16 a[0:15], v[42:45], v[46:49], a[0:15]
	ds_read_b128 v[38:41], v0 offset:192
	ds_read_b128 v[42:45], v0 offset:224
	s_waitcnt lgkmcnt(1)
	v_mfma_f32_32x32x16_f16 a[0:15], v[38:41], v[34:37], a[0:15]
	ds_read_b128 v[34:37], v0 offset:256
	ds_read_b128 v[38:41], v0 offset:288
	s_waitcnt lgkmcnt(2)
	v_mfma_f32_32x32x16_f16 a[0:15], v[42:45], v[62:65], a[0:15]
	s_waitcnt lgkmcnt(1)
	v_mfma_f32_32x32x16_f16 a[0:15], v[34:37], v[26:29], a[0:15]
	s_waitcnt lgkmcnt(0)
	v_mfma_f32_32x32x16_f16 a[0:15], v[38:41], v[30:33], a[0:15]
	ds_read_b128 v[26:29], v0 offset:320
	ds_read_b128 v[30:33], v0 offset:352
	s_waitcnt lgkmcnt(1)
	v_mfma_f32_32x32x16_f16 a[0:15], v[26:29], v[14:17], a[0:15]
	s_waitcnt lgkmcnt(0)
	v_mfma_f32_32x32x16_f16 a[0:15], v[30:33], v[10:13], a[0:15]
	ds_read_b128 v[10:13], v0 offset:384
	ds_read_b128 v[14:17], v0 offset:416
	s_waitcnt lgkmcnt(1)
	v_mfma_f32_32x32x16_f16 a[0:15], v[10:13], v[22:25], a[0:15]
	ds_read_b128 v[10:13], v0 offset:448
	s_waitcnt lgkmcnt(1)
	v_mfma_f32_32x32x16_f16 a[0:15], v[14:17], v[18:21], a[0:15]
	ds_read_b128 v[14:17], v0 offset:480
	v_lshl_or_b32 v0, v197, 5, v198
	s_waitcnt lgkmcnt(1)
	v_mfma_f32_32x32x16_f16 a[0:15], v[10:13], v[6:9], a[0:15]
	v_mov_b32_e32 v6, v230
	s_waitcnt lgkmcnt(0)
	v_mfma_f32_32x32x16_f16 a[0:15], v[14:17], v[2:5], a[0:15]
	s_nop 11
	v_accvgpr_read_b32 v2, a0
	v_accvgpr_read_b32 v3, a1
	s_waitcnt vmcnt(0)
	v_add_f32_e32 v2, v6, v2
	v_max_f32_e32 v2, 0, v2
	v_add_f32_e32 v3, v6, v3
	v_add_f32_e32 v2, 0, v2
	v_max_f32_e32 v3, 0, v3
	v_add_f32_e32 v2, v3, v2
	v_accvgpr_read_b32 v3, a2
	v_add_f32_e32 v3, v6, v3
	v_max_f32_e32 v3, 0, v3
	v_add_f32_e32 v2, v3, v2
	v_accvgpr_read_b32 v3, a3
	v_add_f32_e32 v3, v6, v3
	v_max_f32_e32 v3, 0, v3
	v_add_f32_e32 v2, v3, v2
	v_accvgpr_read_b32 v3, a4
	v_add_f32_e32 v3, v6, v3
	v_max_f32_e32 v3, 0, v3
	v_add_f32_e32 v2, v3, v2
	v_accvgpr_read_b32 v3, a5
	v_add_f32_e32 v3, v6, v3
	v_max_f32_e32 v3, 0, v3
	v_add_f32_e32 v2, v3, v2
	v_accvgpr_read_b32 v3, a6
	v_add_f32_e32 v3, v6, v3
	v_max_f32_e32 v3, 0, v3
	v_add_f32_e32 v2, v3, v2
	v_accvgpr_read_b32 v3, a7
	v_add_f32_e32 v3, v6, v3
	v_max_f32_e32 v3, 0, v3
	v_add_f32_e32 v2, v3, v2
	v_accvgpr_read_b32 v3, a8
	v_add_f32_e32 v3, v6, v3
	v_max_f32_e32 v3, 0, v3
	v_add_f32_e32 v2, v3, v2
	v_accvgpr_read_b32 v3, a9
	v_add_f32_e32 v3, v6, v3
	v_max_f32_e32 v3, 0, v3
	v_add_f32_e32 v2, v3, v2
	v_accvgpr_read_b32 v3, a10
	v_add_f32_e32 v3, v6, v3
	v_max_f32_e32 v3, 0, v3
	v_add_f32_e32 v2, v3, v2
	v_accvgpr_read_b32 v3, a11
	v_add_f32_e32 v3, v6, v3
	v_max_f32_e32 v3, 0, v3
	v_add_f32_e32 v2, v3, v2
	v_accvgpr_read_b32 v3, a12
	v_add_f32_e32 v3, v6, v3
	v_max_f32_e32 v3, 0, v3
	v_add_f32_e32 v2, v3, v2
	v_accvgpr_read_b32 v3, a13
	v_add_f32_e32 v3, v6, v3
	v_max_f32_e32 v3, 0, v3
	v_add_f32_e32 v2, v3, v2
	v_accvgpr_read_b32 v3, a14
	v_add_f32_e32 v3, v6, v3
	v_max_f32_e32 v3, 0, v3
	v_add_f32_e32 v2, v3, v2
	v_accvgpr_read_b32 v3, a15
	v_add_f32_e32 v3, v6, v3
	v_max_f32_e32 v3, 0, v3
	v_add_f32_e32 v2, v3, v2
	v_mbcnt_hi_u32_b32 v3, -1, v196
	v_and_b32_e32 v5, 64, v3
	v_xor_b32_e32 v4, 32, v3
	v_add_u32_e32 v5, 64, v5
	v_cmp_lt_i32_e32 vcc, v4, v5
	s_nop 1
	v_cndmask_b32_e32 v3, v3, v4, vcc
	v_lshlrev_b32_e32 v3, 2, v3
	ds_bpermute_b32 v3, v3, v2
	v_cmp_gt_u32_e32 vcc, 32, v1
	s_and_saveexec_b64 s[4:5], vcc
	s_cbranch_execz .LBB3_11
	s_load_dwordx2 s[0:1], s[0:1], 0x50
	s_ashr_i32 s2, s2, 1
	s_and_b32 s2, s2, 0xffffff80
	v_or_b32_e32 v0, s2, v0
	v_ashrrev_i32_e32 v1, 31, v0
	s_waitcnt lgkmcnt(0)
	v_add_f32_e32 v2, v2, v3
	v_lshl_add_u64 v[0:1], v[0:1], 2, s[0:1]
	global_atomic_add_f32 v[0:1], v2, off

_Z11head_kernelPKfS0_S0_Pf:
	s_load_dwordx4 s[4:7], s[0:1], 0x0
	s_load_dwordx2 s[2:3], s[0:1], 0x18
	s_load_dwordx2 s[10:11], s[0:1], 0x10
	v_mul_lo_u16_e32 v38, 0xcd, v0
	v_lshrrev_b16_e32 v38, 11, v38
	v_mul_i32_i24_e32 v38, -10, v38
	v_add_lshl_u32 v38, v38, v0, 2
	v_mov_b32_e32 v5, 0
	v_lshlrev_b32_e32 v4, 2, v0
	s_movk_i32 s8, 0x1000
	s_waitcnt lgkmcnt(0)
	v_lshl_add_u64 v[2:3], s[4:5], 0, v[4:5]
	v_add_co_u32_e32 v2, vcc, s8, v2
	v_or_b32_e32 v1, 0x1000, v4
	s_nop 0
	v_addc_co_u32_e32 v3, vcc, 0, v3, vcc
	global_load_dword v6, v4, s[4:5]
	global_load_dword v7, v4, s[4:5] offset:1024
	global_load_dword v8, v4, s[4:5] offset:2048
	global_load_dword v9, v4, s[6:7] offset:1024
	global_load_dword v10, v4, s[6:7]
	global_load_dword v11, v4, s[4:5] offset:3072
	global_load_dword v12, v4, s[6:7] offset:3072
	global_load_dword v13, v4, s[6:7] offset:2048
	global_load_dword v14, v1, s[4:5]
	global_load_dword v15, v1, s[6:7]
	global_load_dword v16, v[2:3], off offset:1024
	global_load_dword v17, v[2:3], off offset:2048
	global_load_dword v18, v[2:3], off offset:3072
	global_load_dword v38, v38, s[10:11]
	s_movk_i32 s4, 0xa0
	s_mov_b32 s6, 0
	v_cmp_gt_u32_e32 vcc, s4, v0
	s_waitcnt vmcnt(12)
	ds_write2st64_b32 v4, v6, v7 offset1:4
	s_waitcnt vmcnt(8)
	ds_write2st64_b32 v4, v8, v11 offset0:8 offset1:12
	ds_write2st64_b32 v4, v10, v9 offset0:32 offset1:36
	s_waitcnt vmcnt(6)
	ds_write2st64_b32 v4, v13, v12 offset0:40 offset1:44
	s_waitcnt vmcnt(4)
	ds_write_b32 v4, v15 offset:12288
	s_waitcnt vmcnt(3)
	ds_write2st64_b32 v4, v14, v16 offset0:16 offset1:20
	s_waitcnt vmcnt(0)
	ds_write2st64_b32 v4, v17, v18 offset0:24 offset1:28
	s_waitcnt lgkmcnt(0)
	s_barrier
	s_and_saveexec_b64 s[4:5], vcc
	s_cbranch_execz .LBB7_4
	v_mul_lo_u16_e32 v1, 0xcd, v0
	v_lshrrev_b16_e32 v2, 11, v1
	v_or_b32_e32 v3, 0x2000, v4
	v_mul_i32_i24_e32 v1, -10, v2
	v_lshlrev_b32_e32 v2, 9, v2
	v_lshl_add_u32 v3, v1, 2, v3
.LBB7_2:
	v_add_u32_e32 v18, s6, v2
	ds_read2_b32 v[22:23], v3 offset1:10
	ds_read2_b32 v[24:25], v3 offset0:20 offset1:30
	ds_read2_b32 v[26:27], v3 offset0:40 offset1:50
	ds_read2_b32 v[28:29], v3 offset0:60 offset1:70
	ds_read2_b32 v[30:31], v3 offset0:80 offset1:90
	ds_read2_b32 v[32:33], v3 offset0:100 offset1:110
	ds_read2_b32 v[34:35], v3 offset0:120 offset1:130
	ds_read2_b32 v[36:37], v3 offset0:140 offset1:150
	ds_read_b128 v[6:9], v18
	ds_read_b128 v[10:13], v18 offset:16
	ds_read_b128 v[14:17], v18 offset:32
	ds_read_b128 v[18:21], v18 offset:48
	s_add_i32 s6, s6, 64
	s_waitcnt lgkmcnt(0)
	v_fmac_f32_e32 v5, v6, v22
	v_fmac_f32_e32 v5, v7, v23
	v_fmac_f32_e32 v5, v8, v24
	v_fmac_f32_e32 v5, v9, v25
	v_fmac_f32_e32 v5, v10, v26
	v_fmac_f32_e32 v5, v11, v27
	v_fmac_f32_e32 v5, v12, v28
	v_fmac_f32_e32 v5, v13, v29
	v_fmac_f32_e32 v5, v14, v30
	v_fmac_f32_e32 v5, v15, v31
	v_fmac_f32_e32 v5, v16, v32
	v_fmac_f32_e32 v5, v17, v33
	v_fmac_f32_e32 v5, v18, v34
	v_fmac_f32_e32 v5, v19, v35
	v_fmac_f32_e32 v5, v20, v36
	v_add_u32_e32 v3, 0x280, v3
	s_cmpk_eq_i32 s6, 0x200
	v_fmac_f32_e32 v5, v21, v37
	s_cbranch_scc0 .LBB7_2
	v_fmamk_f32 v1, v5, 0x3b800000, v38
	ds_write_b32 v4, v1 offset:13312

	.amdhsa_kernel _Z11head_kernelPKfS0_S0_Pf
		.amdhsa_group_segment_fixed_size 13952
		.amdhsa_private_segment_fixed_size 0
		.amdhsa_kernarg_size 32
		.amdhsa_user_sgpr_count 2
		.amdhsa_user_sgpr_dispatch_ptr 0
		.amdhsa_user_sgpr_queue_ptr 0
		.amdhsa_user_sgpr_kernarg_segment_ptr 1
		.amdhsa_user_sgpr_dispatch_id 0
		.amdhsa_user_sgpr_kernarg_preload_length 0
		.amdhsa_user_sgpr_kernarg_preload_offset 0
		.amdhsa_user_sgpr_private_segment_size 0
		.amdhsa_uses_dynamic_stack 0
		.amdhsa_enable_private_segment 0
		.amdhsa_system_sgpr_workgroup_id_x 1
		.amdhsa_system_sgpr_workgroup_id_y 0
		.amdhsa_system_sgpr_workgroup_id_z 0
		.amdhsa_system_sgpr_workgroup_info 0
		.amdhsa_system_vgpr_workitem_id 0
		.amdhsa_next_free_vgpr 39
		.amdhsa_next_free_sgpr 12
		.amdhsa_accum_offset 40
		.amdhsa_reserve_vcc 1
		.amdhsa_float_round_mode_32 0
		.amdhsa_float_round_mode_16_64 0
		.amdhsa_float_denorm_mode_32 3
		.amdhsa_float_denorm_mode_16_64 3
		.amdhsa_dx10_clamp 1
		.amdhsa_ieee_mode 1
		.amdhsa_fp16_overflow 0
		.amdhsa_tg_split 0
		.amdhsa_exception_fp_ieee_invalid_op 0
		.amdhsa_exception_fp_denorm_src 0
		.amdhsa_exception_fp_ieee_div_zero 0
		.amdhsa_exception_fp_ieee_overflow 0
		.amdhsa_exception_fp_ieee_underflow 0
		.amdhsa_exception_fp_ieee_inexact 0
		.amdhsa_exception_int_div_zero 0
	.end_amdhsa_kernel

.LBB9_4:
	v_add_u32_e32 v0, 0xa200, v194
	global_load_dword v236, v[162:163], off
	global_load_dword v235, v[162:163], off offset:1024
	global_load_dword v233, v[162:163], off offset:1152
	global_load_dword v234, v[162:163], off offset:128
	v_readfirstlane_b32 s30, v0
	v_add_u32_e32 v0, 0xb200, v194
	s_mov_b32 m0, s30
	v_readfirstlane_b32 s30, v0
	v_add_u32_e32 v0, 0xc200, v194
	global_load_lds_dwordx4 v[164:165], off
	s_mov_b32 m0, s30
	v_readfirstlane_b32 s30, v0
	v_add_u32_e32 v0, 0xd200, v194
	global_load_lds_dwordx4 v[166:167], off
	s_mov_b32 m0, s30
	v_readfirstlane_b32 s30, v0
	global_load_lds_dwordx4 v[168:169], off
	s_mov_b32 m0, s30
	s_or_b32 s49, s14, s33
	global_load_lds_dwordx4 v[170:171], off
	global_load_dwordx4 v[32:35], v[172:173], off
	global_load_dwordx4 v[36:39], v[172:173], off offset:32
	global_load_dwordx4 v[40:43], v[172:173], off offset:2048
	global_load_dwordx4 v[44:47], v[172:173], off offset:2080
	s_lshl_b32 s14, s49, 4
	s_add_i32 s36, s14, -2
	v_mov_b32_e32 v0, 0
	v_mov_b32_e32 v1, 0
	v_mov_b32_e32 v2, 0
	v_mov_b32_e32 v3, 0
	v_mov_b32_e32 v4, 0
	v_add_u32_e32 v160, s36, v196
	v_cmp_gt_u32_e32 vcc, s40, v160
	v_lshl_add_u64 v[6:7], v[160:161], 2, v[174:175]
	s_and_b64 s[38:39], s[0:1], vcc
	s_and_saveexec_b64 s[30:31], s[38:39]
	global_load_dword v1, v[6:7], off
	s_mov_b64 exec, s[30:31]
	v_add_u32_e32 v160, s36, v197
	v_cmp_gt_u32_e32 vcc, s40, v160
	v_lshl_add_u64 v[8:9], v[160:161], 2, v[176:177]
	s_and_b64 s[38:39], s[22:23], vcc
	s_and_saveexec_b64 s[30:31], s[38:39]
	global_load_dword v0, v[8:9], off
	s_mov_b64 exec, s[30:31]
	v_add_u32_e32 v160, s36, v198
	v_cmp_gt_u32_e32 vcc, s40, v160
	v_lshl_add_u64 v[10:11], v[160:161], 2, v[178:179]
	s_and_b64 s[38:39], s[24:25], vcc
	s_and_saveexec_b64 s[30:31], s[38:39]
	global_load_dword v3, v[10:11], off
	s_mov_b64 exec, s[30:31]
	v_add_u32_e32 v160, s36, v199
	v_cmp_gt_u32_e32 vcc, s40, v160
	v_lshl_add_u64 v[12:13], v[160:161], 2, v[180:181]
	s_and_b64 s[38:39], s[26:27], vcc
	s_and_saveexec_b64 s[30:31], s[38:39]
	global_load_dword v2, v[12:13], off
	s_mov_b64 exec, s[30:31]
	v_add_u32_e32 v160, s36, v200
	v_cmp_gt_u32_e32 vcc, s40, v160
	v_lshl_add_u64 v[14:15], v[160:161], 2, v[182:183]
	s_and_b64 s[38:39], s[28:29], vcc
	s_and_saveexec_b64 s[30:31], s[38:39]
	global_load_dword v4, v[14:15], off
	s_mov_b64 exec, s[30:31]
	s_waitcnt vmcnt(0)
	v_cvt_f16_f32_e32 v1, v1
	v_cvt_f16_f32_e32 v0, v0
	v_cvt_f16_f32_e32 v3, v3
	v_cvt_f16_f32_e32 v2, v2
	v_cvt_f16_f32_e32 v4, v4
	ds_write_b16 v201, v1 offset:57856
	s_and_saveexec_b64 s[30:31], s[2:3]
	ds_write_b16 v201, v0 offset:58368
	s_mov_b64 exec, s[30:31]
	s_and_saveexec_b64 s[30:31], s[4:5]
	ds_write_b16 v201, v3 offset:58880
	s_mov_b64 exec, s[30:31]
	s_and_saveexec_b64 s[30:31], s[6:7]
	ds_write_b16 v201, v2 offset:59392
	s_mov_b64 exec, s[30:31]
	s_and_saveexec_b64 s[30:31], s[8:9]
	ds_write_b16 v201, v4 offset:59904

.LBB9_21:
	s_nop 1
	v_mov_b32_e32 v0, 0x143
	v_cmp_gt_u32_e32 vcc, s42, v50
	v_mov_b32_e32 v59, 0x3c00
	s_nop 0
	v_cndmask_b32_e32 v0, v0, v50, vcc
	v_mul_hi_u32 v1, v0, s43
	v_lshrrev_b32_e32 v53, 2, v1
	v_mad_u64_u32 v[48:49], s[38:39], v53, s44, v[0:1]
	v_mul_lo_u32 v0, v53, 40
	v_lshl_add_u32 v4, v48, 1, v0
	v_cndmask_b32_e64 v0, 42, 0, s[12:13]
	v_lshl_add_u32 v0, v0, 1, v4
	v_lshl_add_u32 v1, v202, 1, v4
	v_lshl_add_u32 v2, v203, 1, v4
	v_lshl_add_u32 v3, v204, 1, v4
	v_lshl_add_u32 v5, v205, 1, v4
	v_lshl_add_u32 v6, v206, 1, v4
	v_lshl_add_u32 v7, v207, 1, v4
	v_lshl_add_u32 v8, v208, 1, v4
	ds_read_u16 v0, v0 offset:57856
	ds_read_u16 v1, v1 offset:57856
	ds_read_u16 v2, v2 offset:57856
	ds_read_u16 v3, v3 offset:57856
	ds_read_u16 v5, v5 offset:57856
	ds_read_u16 v6, v6 offset:57856
	ds_read_u16 v7, v7 offset:57856
	ds_read_u16 v8, v8 offset:57856
	v_lshl_add_u32 v9, v209, 1, v4
	v_lshl_add_u32 v10, v210, 1, v4
	v_lshl_add_u32 v11, v211, 1, v4
	v_lshl_add_u32 v12, v212, 1, v4
	v_lshl_add_u32 v13, v213, 1, v4
	v_lshl_add_u32 v14, v214, 1, v4
	v_lshl_add_u32 v15, v215, 1, v4
	v_lshl_add_u32 v58, v216, 1, v4
	ds_read_u16 v9, v9 offset:57856
	ds_read_u16 v10, v10 offset:57856
	ds_read_u16 v11, v11 offset:57856
	ds_read_u16 v12, v12 offset:57856
	ds_read_u16 v13, v13 offset:57856
	ds_read_u16 v14, v14 offset:57856
	ds_read_u16 v15, v15 offset:57856
	ds_read_u16 v58, v58 offset:57856
	v_add_u32_e32 v49, s41, v53
	v_add_u32_e32 v54, s14, v48
	v_max_u32_e32 v49, v49, v54
	v_cmp_gt_u32_e64 s[50:51], s40, v49
	v_lshlrev_b32_e32 v68, 6, v53
	v_lshl_add_u32 v68, v48, 3, v68
	v_and_b32_e32 v68, 0x70, v68
	s_waitcnt lgkmcnt(8)
	v_perm_b32 v60, v1, v0, s45
	v_perm_b32 v61, v3, v2, s45
	v_perm_b32 v62, v6, v5, s45
	v_perm_b32 v63, v8, v7, s45
	v_cndmask_b32_e64 v60, 0, v60, s[50:51]
	v_cndmask_b32_e64 v61, 0, v61, s[50:51]
	v_cndmask_b32_e64 v62, 0, v62, s[50:51]
	v_cndmask_b32_e64 v63, 0, v63, s[50:51]
	s_waitcnt lgkmcnt(0)
	v_cndmask_b32_e64 v12, v59, v12, s[12:13]
	v_perm_b32 v64, v10, v9, s45
	v_perm_b32 v65, v12, v11, s45
	v_perm_b32 v66, v14, v13, s45
	v_perm_b32 v67, v58, v15, s45
	v_mfma_f32_32x32x16_f16 v[16:31], v[32:35], v[60:63], 0
	v_cndmask_b32_e64 v64, 0, v64, s[50:51]
	v_cndmask_b32_e64 v65, 0, v65, s[50:51]
	v_cndmask_b32_e64 v66, 0, v66, s[50:51]
	v_cndmask_b32_e64 v67, 0, v67, s[50:51]
	v_mfma_f32_32x32x16_f16 v[0:15], v[40:43], v[60:63], 0
	s_nop 0
	v_mfma_f32_32x32x16_f16 v[16:31], v[36:39], v[64:67], v[16:31]
	v_mfma_f32_32x32x16_f16 v[0:15], v[44:47], v[64:67], v[0:15]
	s_and_saveexec_b64 s[38:39], vcc
	s_cbranch_execz .LBB9_20
	v_add_u32_e32 v69, v51, v68
	v_xad_u32 v72, v68, 16, v51
	v_xad_u32 v73, v68, 32, v51
	v_xad_u32 v74, v68, 48, v51
	v_xad_u32 v75, v68, 64, v51
	v_xad_u32 v76, v68, s47, v51
	v_xad_u32 v77, v68, s48, v51
	v_xad_u32 v78, v68, s46, v51
	s_nop 1
	v_max_f32_e32 v16, 0, v16
	v_max_f32_e32 v17, 0, v17
	v_max_f32_e32 v18, 0, v18
	v_max_f32_e32 v19, 0, v19
	v_max_f32_e32 v20, 0, v20
	v_max_f32_e32 v21, 0, v21
	v_max_f32_e32 v22, 0, v22
	v_max_f32_e32 v23, 0, v23
	v_cvt_pk_f16_f32 v16, v16, v17
	v_cvt_pk_f16_f32 v17, v18, v19
	v_cvt_pk_f16_f32 v20, v20, v21
	v_cvt_pk_f16_f32 v21, v22, v23
	ds_write_b64 v69, v[16:17]
	ds_write_b64 v72, v[20:21]
	v_max_f32_e32 v24, 0, v24
	v_max_f32_e32 v25, 0, v25
	v_max_f32_e32 v26, 0, v26
	v_max_f32_e32 v27, 0, v27
	v_max_f32_e32 v28, 0, v28
	v_max_f32_e32 v29, 0, v29
	v_max_f32_e32 v30, 0, v30
	v_max_f32_e32 v31, 0, v31
	v_cvt_pk_f16_f32 v24, v24, v25
	v_cvt_pk_f16_f32 v25, v26, v27
	v_cvt_pk_f16_f32 v28, v28, v29
	v_cvt_pk_f16_f32 v29, v30, v31
	ds_write_b64 v73, v[24:25]
	ds_write_b64 v74, v[28:29]
	v_max_f32_e32 v0, 0, v0
	v_max_f32_e32 v1, 0, v1
	v_max_f32_e32 v2, 0, v2
	v_max_f32_e32 v3, 0, v3
	v_max_f32_e32 v4, 0, v4
	v_max_f32_e32 v5, 0, v5
	v_max_f32_e32 v6, 0, v6
	v_max_f32_e32 v7, 0, v7
	v_cvt_pk_f16_f32 v0, v0, v1
	v_cvt_pk_f16_f32 v1, v2, v3
	v_cvt_pk_f16_f32 v4, v4, v5
	v_cvt_pk_f16_f32 v5, v6, v7
	ds_write_b64 v75, v[0:1]
	ds_write_b64 v76, v[4:5]
	v_max_f32_e32 v8, 0, v8
	v_max_f32_e32 v9, 0, v9
	v_max_f32_e32 v10, 0, v10
	v_max_f32_e32 v11, 0, v11
	v_max_f32_e32 v12, 0, v12
	v_max_f32_e32 v13, 0, v13
	v_max_f32_e32 v14, 0, v14
	v_max_f32_e32 v15, 0, v15
	v_cvt_pk_f16_f32 v8, v8, v9
	v_cvt_pk_f16_f32 v9, v10, v11
	v_cvt_pk_f16_f32 v12, v12, v13
	v_cvt_pk_f16_f32 v13, v14, v15
	ds_write_b64 v77, v[8:9]
	ds_write_b64 v78, v[12:13]
	s_branch .LBB9_20

.LBB9_25:
	s_add_i32 s50, s34, -9
	s_cmp_gt_i32 s34, 8
	s_cselect_b64 s[36:37], -1, 0
	s_and_b64 s[38:39], s[36:37], exec
	s_cselect_b32 s38, s50, s34
	s_cmp_lg_u64 s[36:37], 0
	s_mul_hi_i32 s37, s38, 0x55555556
	s_addc_u32 s36, s35, 0
	s_lshr_b32 s39, s37, 31
	s_add_i32 s37, s37, s39
	s_mul_i32 s39, s37, -3
	s_add_i32 s39, s39, s38
	s_waitcnt lgkmcnt(0)
	v_mfma_f32_32x32x16_f16 v[96:111], v[144:147], v[136:139], v[96:111]
	v_lshl_or_b32 v238, s36, 3, v195
	s_mov_b32 s36, 9
	v_mfma_f32_32x32x16_f16 v[32:47], v[144:147], v[132:135], v[32:47]
	v_add_u32_e32 v145, s39, v217
	v_add_u32_e32 v144, s37, v218
	v_lshrrev_b32_e32 v146, 1, v145
	s_lshl_b32 s37, s14, 14
	v_lshl_add_u32 v239, v144, 2, v146
	v_mul_lo_u32 v144, v144, 18
	s_and_b32 s37, s37, 0x4000
	v_add_lshl_u32 v160, v145, v144, 7
	v_or_b32_e32 v237, s37, v219
	v_bitop3_b32 v144, v239, v238, 7 bitop3:0x6c
	v_mfma_f32_32x32x16_f16 v[112:127], v[148:151], v[136:139], v[112:127]
	v_add_u32_e32 v145, v237, v220
	v_lshl_add_u32 v144, v144, 4, v160
	s_cmp_eq_u32 s14, 8
	v_mfma_f32_32x32x16_f16 v[64:79], v[148:151], v[132:135], v[64:79]
	v_mfma_f32_32x32x16_f16 v[80:95], v[140:143], v[136:139], v[80:95]
	v_mfma_f32_32x32x16_f16 v[16:31], v[140:143], v[132:135], v[16:31]
	v_mfma_f32_32x32x16_f16 v[48:63], v[128:131], v[136:139], v[48:63]
	ds_read_b128 v[140:143], v145 offset:41472
	ds_read_b128 v[136:139], v145 offset:45568
	ds_read_b128 v[156:159], v144
	ds_read_b128 v[152:155], v144 offset:4608
	ds_read_b128 v[148:151], v144 offset:9216
	ds_read_b128 v[144:147], v144 offset:13824
	v_mfma_f32_32x32x16_f16 v[0:15], v[128:131], v[132:135], v[0:15]
	s_cbranch_scc1 .LBB9_24
	s_add_i32 s36, s14, 1
	s_lshl_b32 s14, s36, 14
	s_and_b32 s37, s14, 0x4000
	v_or_b32_e32 v134, s37, v194
	v_add_u32_e32 v240, 0xa200, v134
	v_lshl_add_u64 v[128:129], v[164:165], 0, s[14:15]
	v_add_u32_e32 v243, 0xb200, v134
	v_readfirstlane_b32 s14, v240
	v_add_u32_e32 v242, 0xc200, v134
	s_mov_b32 m0, s14
	v_readfirstlane_b32 s14, v243
	v_add_u32_e32 v241, 0xd200, v134
	v_lshl_add_u64 v[134:135], v[128:129], 0, s[16:17]
	global_load_lds_dwordx4 v[128:129], off
	s_mov_b32 m0, s14
	v_readfirstlane_b32 s14, v242
	v_lshl_add_u64 v[132:133], v[128:129], 0, s[18:19]
	global_load_lds_dwordx4 v[134:135], off
	s_mov_b32 m0, s14
	v_readfirstlane_b32 s14, v241
	v_lshl_add_u64 v[130:131], v[128:129], 0, s[20:21]
	global_load_lds_dwordx4 v[132:133], off
	s_mov_b32 m0, s14
	s_nop 0
	global_load_lds_dwordx4 v[130:131], off
	s_branch .LBB9_24
.LBB9_31:
	s_endpgm
	s_endpgm
	s_endpgm
	s_endpgm
	s_endpgm
	s_endpgm
	s_endpgm
	s_endpgm
	s_endpgm
	s_endpgm
	s_endpgm
	s_endpgm
	s_endpgm
	s_endpgm
	s_endpgm
	s_endpgm
	s_endpgm
	s_endpgm
	s_endpgm
	s_endpgm
	s_endpgm
	s_endpgm
	s_endpgm
	s_endpgm
	s_endpgm
	s_endpgm
	s_endpgm
	s_endpgm
	s_endpgm
	s_endpgm
	s_endpgm
	s_endpgm
	s_endpgm
	s_endpgm
	s_endpgm
	s_endpgm
	s_endpgm
	s_endpgm
	s_endpgm
	s_endpgm
	.section	.rodata,"a",@progbits
	.p2align	6, 0x0
